# P7: list2 indices fetched before the last sub-phase's LDS-DMA prefetches, epilogue waits vmcnt(6) only; sites 1-2 after epilogue relaxed
# speedup vs baseline: 1.0068x; 1.0068x over previous
; #define PG8_STAGE(bufoff, gbase, voff) do { _Pragma("unroll") for (int _i = 0; _i < 2; ++_i) { unsigned keep_; \
;         asm volatile("s_mov_b32 %0, m0\n\ts_mov_b32 m0, %3\n\ts_nop 0\n\tglobal_load_lds_dwordx4 %1, %2\n\ts_mov_b32 m0, %0" : "=&s"(keep_) : "v"((voff)[_i]), "s"((const char*)(gbase)), "s"(ldsb + (unsigned)((bufoff) + _i * 8192)) : "memory"); } } while (0)
; #define PG8_LDA(dst, b, h) do { _Pragma("unroll") for (int m = 0; m < 4; ++m) _Pragma("unroll") for (int k = 0; k < 2; ++k) dst[m][k] = *(const PG8_LAS bf16x8*)(lds + PG8_SA(b, h) + aoff + m * 2048 + k * 1024); } while (0)
; #define PG8_LDB(dst, b, h) do { _Pragma("unroll") for (int n = 0; n < 2; ++n) _Pragma("unroll") for (int k = 0; k < 2; ++k) dst[n][k] = *(const PG8_LAS bf16x8*)(lds + PG8_SB(b, h) + boff + n * 2048 + k * 1024); } while (0)
; #define PG8_WAIT_V(n) asm volatile("s_waitcnt vmcnt(" #n ")" ::: "memory")
; #define PG8_WAIT_L(n) asm volatile("s_waitcnt lgkmcnt(" #n ")" ::: "memory")
; #define PG8_BAR __builtin_amdgcn_s_barrier()
; #define PG8_SCHED __builtin_amdgcn_sched_barrier(0)
; template <class Epi, class Sched, bool ALIGN_EPI, bool FP8 = false>
; __device__ __forceinline__ void gemm_phase(PG8_LAS unsigned char* lds, const Gemm g, const Sched& S, const Epi& E, const int wid, const int lane) {
;     ...
;             PG8_WAIT_V(8); PG8_WAIT_L(0); PG8_BAR; PG8_MMA(1, 0, At, B0); PG8_MMA(1, 1, At, B1); PG8_BAR; PG8_SCHED;
;             PG8_LDB(B0, 1, 0); PG8_LDB(B1, 1, 1); PG8_SCHED; PG8_LDA(At, 1, 0); PG8_STAGE(PG8_SA(0, 1), a2 + hstepA, vc1);
;             PG8_WAIT_V(8); PG8_WAIT_L(0); PG8_BAR; PG8_MMA(0, 0, At, B0); PG8_MMA(0, 1, At, B1); PG8_BAR; PG8_SCHED;
;     __device__ __forceinline__ void operator()(const f32x4 (&acc)[2][2][4][2], const Unit& u, int wr, int wc, int fr, int fq) const {
;     ...
;         const int e = tileE[u.pm], lbase = (u.pm - tb[e]) * 256 + wr * 64 + fr, ce = cnt[e];
;         const float ysc = (float)(1 << YSHIFT);
;         int drow[2][4];
; #pragma unroll
;         for (int ai = 0; ai < 2; ++ai)
; #pragma unroll
;             for (int m = 0; m < 4; ++m) { const int local = lbase + ai * HALF + m * 16; drow[ai][m] = (e >= NE) ? (local * 7 + 6) : ((local < ce) ? list2[(size_t)e * LISTCAP + local] : 7 * T); }
.Lrxj7_1:
	s_mov_b32 s101, 0
	s_waitcnt lgkmcnt(0)
	s_barrier
	s_setprio 1
	s_waitcnt lgkmcnt(6)
	v_mfma_scale_f32_16x16x128_f8f6f4 v[92:95], v[24:31], v[174:181], v[92:95], v170, v171 op_sel_hi:[0,0,0]
	v_mfma_scale_f32_16x16x128_f8f6f4 v[88:91], v[16:23], v[174:181], v[88:91], v170, v171 op_sel_hi:[0,0,0]
	s_waitcnt lgkmcnt(4)
	v_mfma_scale_f32_16x16x128_f8f6f4 v[76:79], v[24:31], v[182:189], v[76:79], v170, v171 op_sel_hi:[0,0,0]
	v_mfma_scale_f32_16x16x128_f8f6f4 v[72:75], v[16:23], v[182:189], v[72:75], v170, v171 op_sel_hi:[0,0,0]
	s_waitcnt lgkmcnt(2)
	v_mfma_scale_f32_16x16x128_f8f6f4 v[60:63], v[24:31], v[190:197], v[60:63], v170, v171 op_sel_hi:[0,0,0]
	v_mfma_scale_f32_16x16x128_f8f6f4 v[56:59], v[16:23], v[190:197], v[56:59], v170, v171 op_sel_hi:[0,0,0]
	s_waitcnt lgkmcnt(0)
	v_mfma_scale_f32_16x16x128_f8f6f4 v[44:47], v[24:31], v[198:205], v[44:47], v170, v171 op_sel_hi:[0,0,0]
	v_mfma_scale_f32_16x16x128_f8f6f4 v[40:43], v[16:23], v[198:205], v[40:43], v170, v171 op_sel_hi:[0,0,0]
	s_setprio 0
	s_setprio 1
	v_mfma_scale_f32_16x16x128_f8f6f4 v[84:87], v[8:15], v[174:181], v[84:87], v170, v171 op_sel_hi:[0,0,0]
	v_mfma_scale_f32_16x16x128_f8f6f4 v[80:83], v[0:7], v[174:181], v[80:83], v170, v171 op_sel_hi:[0,0,0]
	v_mfma_scale_f32_16x16x128_f8f6f4 v[68:71], v[8:15], v[182:189], v[68:71], v170, v171 op_sel_hi:[0,0,0]
	v_mfma_scale_f32_16x16x128_f8f6f4 v[64:67], v[0:7], v[182:189], v[64:67], v170, v171 op_sel_hi:[0,0,0]
	v_mfma_scale_f32_16x16x128_f8f6f4 v[52:55], v[8:15], v[190:197], v[52:55], v170, v171 op_sel_hi:[0,0,0]
	v_mfma_scale_f32_16x16x128_f8f6f4 v[48:51], v[0:7], v[190:197], v[48:51], v170, v171 op_sel_hi:[0,0,0]
	v_mfma_scale_f32_16x16x128_f8f6f4 v[36:39], v[8:15], v[198:205], v[36:39], v170, v171 op_sel_hi:[0,0,0]
	v_mfma_scale_f32_16x16x128_f8f6f4 v[32:35], v[0:7], v[198:205], v[32:35], v170, v171 op_sel_hi:[0,0,0]
	s_setprio 0
	s_barrier
	ds_read_b128 v[0:3], v172
	ds_read_b128 v[4:7], v172 offset:1024
	ds_read_b128 v[8:11], v172 offset:2048
	ds_read_b128 v[12:15], v172 offset:3072
	ds_read_b128 v[16:19], v173
	ds_read_b128 v[20:23], v173 offset:1024
	ds_read_b128 v[24:27], v173 offset:2048
	ds_read_b128 v[28:31], v173 offset:3072
	ds_read_b128 v[174:177], v169 offset:32768
	ds_read_b128 v[178:181], v169 offset:33792
	ds_read_b128 v[182:185], v169 offset:34816
	ds_read_b128 v[186:189], v169 offset:35840
	ds_read_b128 v[190:193], v169 offset:36864
	ds_read_b128 v[194:197], v169 offset:37888
	ds_read_b128 v[198:201], v169 offset:38912
	ds_read_b128 v[202:205], v169 offset:39936
	s_add_u32 s36, s36, s12
	s_addc_u32 s37, s37, s13
	s_mov_b32 m0, s50
	s_nop 0
	global_load_lds_dwordx4 v160, s[36:37]
	s_mov_b32 m0, s51
	s_nop 0
	global_load_lds_dwordx4 v164, s[36:37]
	s_waitcnt vmcnt(8)
	s_waitcnt lgkmcnt(0)
	s_barrier
	s_setprio 1
	s_waitcnt lgkmcnt(6)
	v_mfma_scale_f32_16x16x128_f8f6f4 v[156:159], v[0:7], v[174:181], v[156:159], v170, v171 op_sel_hi:[0,0,0]
	v_mfma_scale_f32_16x16x128_f8f6f4 v[152:155], v[8:15], v[174:181], v[152:155], v170, v171 op_sel_hi:[0,0,0]
	s_waitcnt lgkmcnt(4)
	v_mfma_scale_f32_16x16x128_f8f6f4 v[140:143], v[0:7], v[182:189], v[140:143], v170, v171 op_sel_hi:[0,0,0]
	v_mfma_scale_f32_16x16x128_f8f6f4 v[136:139], v[8:15], v[182:189], v[136:139], v170, v171 op_sel_hi:[0,0,0]
	s_waitcnt lgkmcnt(2)
	v_mfma_scale_f32_16x16x128_f8f6f4 v[124:127], v[0:7], v[190:197], v[124:127], v170, v171 op_sel_hi:[0,0,0]
	v_mfma_scale_f32_16x16x128_f8f6f4 v[120:123], v[8:15], v[190:197], v[120:123], v170, v171 op_sel_hi:[0,0,0]
	s_waitcnt lgkmcnt(0)
	v_mfma_scale_f32_16x16x128_f8f6f4 v[108:111], v[0:7], v[198:205], v[108:111], v170, v171 op_sel_hi:[0,0,0]
	v_mfma_scale_f32_16x16x128_f8f6f4 v[104:107], v[8:15], v[198:205], v[104:107], v170, v171 op_sel_hi:[0,0,0]
	s_setprio 0
	s_setprio 1
	v_mfma_scale_f32_16x16x128_f8f6f4 v[148:151], v[16:23], v[174:181], v[148:151], v170, v171 op_sel_hi:[0,0,0]
	v_mfma_scale_f32_16x16x128_f8f6f4 v[144:147], v[24:31], v[174:181], v[144:147], v170, v171 op_sel_hi:[0,0,0]
	v_mfma_scale_f32_16x16x128_f8f6f4 v[132:135], v[16:23], v[182:189], v[132:135], v170, v171 op_sel_hi:[0,0,0]
	v_mfma_scale_f32_16x16x128_f8f6f4 v[128:131], v[24:31], v[182:189], v[128:131], v170, v171 op_sel_hi:[0,0,0]
	v_mfma_scale_f32_16x16x128_f8f6f4 v[116:119], v[16:23], v[190:197], v[116:119], v170, v171 op_sel_hi:[0,0,0]
	v_mfma_scale_f32_16x16x128_f8f6f4 v[112:115], v[24:31], v[190:197], v[112:115], v170, v171 op_sel_hi:[0,0,0]
	v_mfma_scale_f32_16x16x128_f8f6f4 v[100:103], v[16:23], v[198:205], v[100:103], v170, v171 op_sel_hi:[0,0,0]
	v_mfma_scale_f32_16x16x128_f8f6f4 v[96:99], v[24:31], v[198:205], v[96:99], v170, v171 op_sel_hi:[0,0,0]
	s_setprio 0
	s_barrier
	s_cmp_lt_i32 s33, s52
	s_cbranch_scc1 .Lp7a_skip
	s_lshl_b32 s98, s74, 2
	s_add_i32 s98, s98, 0x20800
	v_mov_b32_e32 v206, s98
	ds_read_b32 v211, v206
	s_waitcnt lgkmcnt(0)
	s_nop 0
	v_readfirstlane_b32 s98, v211
	s_nop 3
	s_lshl_b32 s100, s98, 2
	s_add_i32 s99, s100, 0x21000
	s_add_i32 s100, s100, 0x21200
	v_mov_b32_e32 v206, s99
	v_mov_b32_e32 v207, s100
	ds_read_b32 v206, v206
	ds_read_b32 v207, v207
	s_ashr_i32 s99, s98, 31
	s_lshl_b64 s[98:99], s[98:99], 16
	s_add_u32 s98, s20, s98
	s_addc_u32 s99, s21, s99
	s_waitcnt lgkmcnt(0)
	v_sub_u32_e32 v206, s74, v206
	v_lshl_add_u32 v208, v206, 8, v161
	v_add_u32_e32 v209, 0, v208
	v_lshlrev_b32_e32 v238, 2, v209
	global_load_dword v230, v238, s[98:99]
	v_add_u32_e32 v209, 16, v208
	v_lshlrev_b32_e32 v239, 2, v209
	global_load_dword v231, v239, s[98:99]
	v_add_u32_e32 v209, 32, v208
	v_lshlrev_b32_e32 v240, 2, v209
	global_load_dword v232, v240, s[98:99]
	v_add_u32_e32 v209, 48, v208
	v_lshlrev_b32_e32 v241, 2, v209
	global_load_dword v233, v241, s[98:99]
	v_add_u32_e32 v209, 0x80, v208
	v_lshlrev_b32_e32 v242, 2, v209
	global_load_dword v234, v242, s[98:99]
	v_add_u32_e32 v209, 0x90, v208
	v_lshlrev_b32_e32 v243, 2, v209
	global_load_dword v235, v243, s[98:99]
	v_add_u32_e32 v209, 0xa0, v208
	v_lshlrev_b32_e32 v244, 2, v209
	global_load_dword v236, v244, s[98:99]
	v_add_u32_e32 v209, 0xb0, v208
	v_lshlrev_b32_e32 v245, 2, v209
	global_load_dword v237, v245, s[98:99]
; #define PG8_STAGE(bufoff, gbase, voff) do { _Pragma("unroll") for (int _i = 0; _i < 2; ++_i) { unsigned keep_; \
;         asm volatile("s_mov_b32 %0, m0\n\ts_mov_b32 m0, %3\n\ts_nop 0\n\tglobal_load_lds_dwordx4 %1, %2\n\ts_mov_b32 m0, %0" : "=&s"(keep_) : "v"((voff)[_i]), "s"((const char*)(gbase)), "s"(ldsb + (unsigned)((bufoff) + _i * 8192)) : "memory"); } } while (0)
; #define PG8_LDA(dst, b, h) do { _Pragma("unroll") for (int m = 0; m < 4; ++m) _Pragma("unroll") for (int k = 0; k < 2; ++k) dst[m][k] = *(const PG8_LAS bf16x8*)(lds + PG8_SA(b, h) + aoff + m * 2048 + k * 1024); } while (0)
; #define PG8_WAIT_V(n) asm volatile("s_waitcnt vmcnt(" #n ")" ::: "memory")
; #define PG8_WAIT_L(n) asm volatile("s_waitcnt lgkmcnt(" #n ")" ::: "memory")
; #define PG8_BAR __builtin_amdgcn_s_barrier()
; #define PG8_SCHED __builtin_amdgcn_sched_barrier(0)
; template <class Epi, class Sched, bool ALIGN_EPI, bool FP8 = false>
; __device__ __forceinline__ void gemm_phase(PG8_LAS unsigned char* lds, const Gemm g, const Sched& S, const Epi& E, const int wid, const int lane) {
;     ...
;             PG8_LDA(At, 1, 1); PG8_STAGE(PG8_SB(1, 0), b3, voffB); PG8_STAGE(PG8_SB(1, 1), b3 + hstep, voffB); PG8_STAGE(PG8_SA(1, 0), a3, vc0);
;             PG8_WAIT_V(8); PG8_WAIT_L(0); PG8_BAR; PG8_MMA(1, 0, At, B0); PG8_MMA(1, 1, At, B1); PG8_BAR; PG8_SCHED;
.Lp7a_skip:
	ds_read_b128 v[174:177], v169 offset:49152
	ds_read_b128 v[178:181], v169 offset:50176
	ds_read_b128 v[182:185], v169 offset:51200
	ds_read_b128 v[186:189], v169 offset:52224
	ds_read_b128 v[190:193], v169 offset:53248
	ds_read_b128 v[194:197], v169 offset:54272
	ds_read_b128 v[198:201], v169 offset:55296
	ds_read_b128 v[202:205], v169 offset:56320
	s_add_u32 s34, s34, 0x80
	s_addc_u32 s35, s35, 0
	s_mov_b32 m0, s53
	s_nop 0
	global_load_lds_dwordx4 v162, s[34:35]
	s_mov_b32 m0, s54
	s_nop 0
	global_load_lds_dwordx4 v166, s[34:35]
	s_add_u32 s34, s34, s12
	s_addc_u32 s35, s35, s13
	s_mov_b32 m0, s65
	s_nop 0
	global_load_lds_dwordx4 v162, s[34:35]
	s_mov_b32 m0, s66
	s_nop 0
	global_load_lds_dwordx4 v166, s[34:35]
	s_mov_b32 m0, s55
	s_nop 0
	global_load_lds_dwordx4 v160, s[8:9]
	s_mov_b32 m0, s64
	s_nop 0
	global_load_lds_dwordx4 v164, s[8:9]
	s_cmp_lt_i32 s33, s52
	s_cbranch_scc1 .Lp7a_w4n
	s_waitcnt vmcnt(16)
	s_branch .Lp7a_w4j

; #define PG8_WAIT_V(n) asm volatile("s_waitcnt vmcnt(" #n ")" ::: "memory")
; #define PG8_WAIT_L(n) asm volatile("s_waitcnt lgkmcnt(" #n ")" ::: "memory")
; #define PG8_BAR __builtin_amdgcn_s_barrier()
; #define PG8_SCHED __builtin_amdgcn_sched_barrier(0)
; template <class Epi, class Sched, bool ALIGN_EPI, bool FP8 = false>
; __device__ __forceinline__ void gemm_phase(PG8_LAS unsigned char* lds, const Gemm g, const Sched& S, const Epi& E, const int wid, const int lane) {
;     ...
;             PG8_WAIT_V(8); PG8_WAIT_L(0); PG8_BAR; PG8_MMA(1, 0, At, B0); PG8_MMA(1, 1, At, B1); PG8_BAR; PG8_SCHED;
;         }
.Lp7a_w4j:
	s_waitcnt lgkmcnt(0)
	s_barrier
	s_setprio 1
	s_waitcnt lgkmcnt(6)
	v_mfma_scale_f32_16x16x128_f8f6f4 v[92:95], v[0:7], v[174:181], v[92:95], v170, v171 op_sel_hi:[0,0,0]
	v_mfma_scale_f32_16x16x128_f8f6f4 v[88:91], v[8:15], v[174:181], v[88:91], v170, v171 op_sel_hi:[0,0,0]
	s_waitcnt lgkmcnt(4)
	v_mfma_scale_f32_16x16x128_f8f6f4 v[76:79], v[0:7], v[182:189], v[76:79], v170, v171 op_sel_hi:[0,0,0]
	v_mfma_scale_f32_16x16x128_f8f6f4 v[72:75], v[8:15], v[182:189], v[72:75], v170, v171 op_sel_hi:[0,0,0]
	s_waitcnt lgkmcnt(2)
	v_mfma_scale_f32_16x16x128_f8f6f4 v[60:63], v[0:7], v[190:197], v[60:63], v170, v171 op_sel_hi:[0,0,0]
	v_mfma_scale_f32_16x16x128_f8f6f4 v[56:59], v[8:15], v[190:197], v[56:59], v170, v171 op_sel_hi:[0,0,0]
	s_waitcnt lgkmcnt(0)
	v_mfma_scale_f32_16x16x128_f8f6f4 v[44:47], v[0:7], v[198:205], v[44:47], v170, v171 op_sel_hi:[0,0,0]
	v_mfma_scale_f32_16x16x128_f8f6f4 v[40:43], v[8:15], v[198:205], v[40:43], v170, v171 op_sel_hi:[0,0,0]
	s_setprio 0
	s_setprio 1
	v_mfma_scale_f32_16x16x128_f8f6f4 v[84:87], v[16:23], v[174:181], v[84:87], v170, v171 op_sel_hi:[0,0,0]
	v_mfma_scale_f32_16x16x128_f8f6f4 v[80:83], v[24:31], v[174:181], v[80:83], v170, v171 op_sel_hi:[0,0,0]
	v_mfma_scale_f32_16x16x128_f8f6f4 v[68:71], v[16:23], v[182:189], v[68:71], v170, v171 op_sel_hi:[0,0,0]
	v_mfma_scale_f32_16x16x128_f8f6f4 v[64:67], v[24:31], v[182:189], v[64:67], v170, v171 op_sel_hi:[0,0,0]
	v_mfma_scale_f32_16x16x128_f8f6f4 v[52:55], v[16:23], v[190:197], v[52:55], v170, v171 op_sel_hi:[0,0,0]
	v_mfma_scale_f32_16x16x128_f8f6f4 v[48:51], v[24:31], v[190:197], v[48:51], v170, v171 op_sel_hi:[0,0,0]
	v_mfma_scale_f32_16x16x128_f8f6f4 v[36:39], v[16:23], v[198:205], v[36:39], v170, v171 op_sel_hi:[0,0,0]
	v_mfma_scale_f32_16x16x128_f8f6f4 v[32:35], v[24:31], v[198:205], v[32:35], v170, v171 op_sel_hi:[0,0,0]
	s_setprio 0
	s_barrier
	s_add_u32 s75, s75, 0x100
	s_addc_u32 s82, s82, 0
	s_add_u32 s83, s83, 0x100
	s_addc_u32 s84, s84, 0
	s_add_u32 s6, s6, 0x100
	s_addc_u32 s7, s7, 0
	s_cmp_ge_i32 s33, s52
	s_mov_b32 s8, s33
	s_cbranch_scc0 .LBB0_852

; __device__ __forceinline__ unsigned pk4_fp8(float a, float b, float c, float d) { int r = __builtin_amdgcn_cvt_pk_fp8_f32(a, b, 0, false); r = __builtin_amdgcn_cvt_pk_fp8_f32(c, d, r, true); return (unsigned)r; }
;     __device__ __forceinline__ void operator()(const f32x4 (&acc)[2][2][4][2], const Unit& u, int wr, int wc, int fr, int fq) const {
;         const int col0 = (u.pn & 7) * 256 + wc * 64 + 16 * fq;
;         const int e = tileE[u.pm], lbase = (u.pm - tb[e]) * 256 + wr * 64 + fr, ce = cnt[e];
;         const float ysc = (float)(1 << YSHIFT);
;         int drow[2][4];
; #pragma unroll
;         for (int ai = 0; ai < 2; ++ai)
; #pragma unroll
;             for (int m = 0; m < 4; ++m) { const int local = lbase + ai * HALF + m * 16; drow[ai][m] = (e >= NE) ? (local * 7 + 6) : ((local < ce) ? list2[(size_t)e * LISTCAP + local] : 7 * T); }
; #pragma unroll
;         for (int ai = 0; ai < 2; ++ai)
; #pragma unroll
;             for (int m = 0; m < 4; ++m) { unsigned char* rowp = O + (size_t)drow[ai][m] * D + col0;
;                 const f32x4 a0 = acc[ai][0][m][0] * ysc, a1 = acc[ai][0][m][1] * ysc, b0 = acc[ai][1][m][0] * ysc, b1 = acc[ai][1][m][1] * ysc;
;                 v4u w; w.x = pk4_fp8(a0[0], a0[1], a0[2], a0[3]); w.y = pk4_fp8(a1[0], a1[1], a1[2], a1[3]); w.z = pk4_fp8(b0[0], b0[1], b0[2], b0[3]); w.w = pk4_fp8(b1[0], b1[1], b1[2], b1[3]);
;                 *(v4u*)rowp = w; }
.LBB0_855:
	s_nop 15
	s_nop 15
	s_waitcnt vmcnt(6)
	v_readfirstlane_b32 s98, v211
	v_mov_b32_e32 v210, 0x1c000
	s_nop 1
	s_cmp_gt_i32 s98, 63
	s_cbranch_scc1 .Lp7a_sh
	v_add_u32_e32 v209, 0, v208
	v_cmp_lt_i32_e32 vcc, v209, v207
	s_nop 1
	v_cndmask_b32_e32 v10, v210, v230, vcc
	v_add_u32_e32 v209, 16, v208
	v_cmp_lt_i32_e32 vcc, v209, v207
	s_nop 1
	v_cndmask_b32_e32 v14, v210, v231, vcc
	v_add_u32_e32 v209, 32, v208
	v_cmp_lt_i32_e32 vcc, v209, v207
	s_nop 1
	v_cndmask_b32_e32 v12, v210, v232, vcc
	v_add_u32_e32 v209, 48, v208
	v_cmp_lt_i32_e32 vcc, v209, v207
	s_nop 1
	v_cndmask_b32_e32 v8, v210, v233, vcc
	v_add_u32_e32 v209, 0x80, v208
	v_cmp_lt_i32_e32 vcc, v209, v207
	s_nop 1
	v_cndmask_b32_e32 v6, v210, v234, vcc
	v_add_u32_e32 v209, 0x90, v208
	v_cmp_lt_i32_e32 vcc, v209, v207
	s_nop 1
	v_cndmask_b32_e32 v4, v210, v235, vcc
	v_add_u32_e32 v209, 0xa0, v208
	v_cmp_lt_i32_e32 vcc, v209, v207
	s_nop 1
	v_cndmask_b32_e32 v2, v210, v236, vcc
	v_add_u32_e32 v209, 0xb0, v208
	v_cmp_lt_i32_e32 vcc, v209, v207
	s_nop 1
	v_cndmask_b32_e32 v0, v210, v237, vcc
	s_branch .Lp7a_j
.Lp7a_sh:
	v_add_u32_e32 v209, 0, v208
	v_mul_u32_u24_e32 v209, 7, v209
	v_add_u32_e32 v10, 6, v209
	v_add_u32_e32 v209, 16, v208
	v_mul_u32_u24_e32 v209, 7, v209
	v_add_u32_e32 v14, 6, v209
	v_add_u32_e32 v209, 32, v208
	v_mul_u32_u24_e32 v209, 7, v209
	v_add_u32_e32 v12, 6, v209
	v_add_u32_e32 v209, 48, v208
	v_mul_u32_u24_e32 v209, 7, v209
	v_add_u32_e32 v8, 6, v209
	v_add_u32_e32 v209, 0x80, v208
	v_mul_u32_u24_e32 v209, 7, v209
	v_add_u32_e32 v6, 6, v209
	v_add_u32_e32 v209, 0x90, v208
	v_mul_u32_u24_e32 v209, 7, v209
	v_add_u32_e32 v4, 6, v209
	v_add_u32_e32 v209, 0xa0, v208
	v_mul_u32_u24_e32 v209, 7, v209
	v_add_u32_e32 v2, 6, v209
	v_add_u32_e32 v209, 0xb0, v208
	v_mul_u32_u24_e32 v209, 7, v209
	v_add_u32_e32 v0, 6, v209
.Lp7a_j:
.LBB0_903:
	v_pk_mul_f32 v[20:21], v[156:157], s[26:27] op_sel_hi:[1,0]
	v_mov_b32_e32 v18, 0
	v_pk_mul_f32 v[26:27], v[152:153], s[26:27] op_sel_hi:[1,0]
	v_pk_mul_f32 v[30:31], v[148:149], s[26:27] op_sel_hi:[1,0]
	v_pk_mul_f32 v[144:145], v[144:145], s[26:27] op_sel_hi:[1,0]
	v_cvt_pk_fp8_f32 v18, v20, v21
	v_mov_b32_e32 v19, 0
	v_mov_b32_e32 v20, 0
	v_mov_b32_e32 v21, 0
	v_cvt_pk_fp8_f32 v19, v26, v27
	v_cvt_pk_fp8_f32 v20, v30, v31
	v_cvt_pk_fp8_f32 v21, v144, v145
	s_lshl_b32 s6, s73, 8
	v_pk_mul_f32 v[22:23], v[158:159], s[26:27] op_sel_hi:[1,0]
	v_pk_mul_f32 v[24:25], v[154:155], s[26:27] op_sel_hi:[1,0]
	v_pk_mul_f32 v[28:29], v[150:151], s[26:27] op_sel_hi:[1,0]
	v_pk_mul_f32 v[146:147], v[146:147], s[26:27] op_sel_hi:[1,0]
	s_and_b32 s6, s6, 0x700
	s_nop 0
	v_ashrrev_i32_e32 v11, 31, v10
	v_cvt_pk_fp8_f32 v18, v22, v23 op_sel:[0,0,1]
	v_cvt_pk_fp8_f32 v19, v24, v25 op_sel:[0,0,1]
	v_cvt_pk_fp8_f32 v20, v28, v29 op_sel:[0,0,1]
	v_cvt_pk_fp8_f32 v21, v146, v147 op_sel:[0,0,1]
	v_add_u32_e32 v16, s6, v163
	v_lshlrev_b64 v[10:11], 11, v[10:11]
	v_ashrrev_i32_e32 v17, 31, v16
	v_lshl_add_u64 v[10:11], s[18:19], 0, v[10:11]
	v_lshl_add_u64 v[10:11], v[10:11], 0, v[16:17]
	global_store_dwordx4 v[10:11], v[18:21], off
	v_pk_mul_f32 v[24:25], v[136:137], s[26:27] op_sel_hi:[1,0]
	v_pk_mul_f32 v[28:29], v[132:133], s[26:27] op_sel_hi:[1,0]
	v_pk_mul_f32 v[20:21], v[140:141], s[26:27] op_sel_hi:[1,0]
	v_mov_b32_e32 v18, 0
	v_pk_mul_f32 v[128:129], v[128:129], s[26:27] op_sel_hi:[1,0]
	v_cvt_pk_fp8_f32 v18, v20, v21
	v_mov_b32_e32 v19, 0
	v_mov_b32_e32 v20, 0
	v_mov_b32_e32 v21, 0
	v_cvt_pk_fp8_f32 v19, v24, v25
	v_cvt_pk_fp8_f32 v20, v28, v29
	v_cvt_pk_fp8_f32 v21, v128, v129
	v_pk_mul_f32 v[10:11], v[142:143], s[26:27] op_sel_hi:[1,0]
	v_pk_mul_f32 v[22:23], v[138:139], s[26:27] op_sel_hi:[1,0]
	v_pk_mul_f32 v[26:27], v[134:135], s[26:27] op_sel_hi:[1,0]
	v_pk_mul_f32 v[30:31], v[130:131], s[26:27] op_sel_hi:[1,0]
	v_ashrrev_i32_e32 v15, 31, v14
	v_cvt_pk_fp8_f32 v18, v10, v11 op_sel:[0,0,1]
	v_cvt_pk_fp8_f32 v19, v22, v23 op_sel:[0,0,1]
	v_cvt_pk_fp8_f32 v20, v26, v27 op_sel:[0,0,1]
	v_cvt_pk_fp8_f32 v21, v30, v31 op_sel:[0,0,1]
	v_lshlrev_b64 v[10:11], 11, v[14:15]
	v_lshl_add_u64 v[10:11], s[18:19], 0, v[10:11]
	v_lshl_add_u64 v[10:11], v[10:11], 0, v[16:17]
	global_store_dwordx4 v[10:11], v[18:21], off
	v_pk_mul_f32 v[14:15], v[124:125], s[26:27] op_sel_hi:[1,0]
	v_pk_mul_f32 v[26:27], v[116:117], s[26:27] op_sel_hi:[1,0]
	v_pk_mul_f32 v[20:21], v[120:121], s[26:27] op_sel_hi:[1,0]
	v_mov_b32_e32 v19, 0
	v_pk_mul_f32 v[30:31], v[112:113], s[26:27] op_sel_hi:[1,0]
	v_mov_b32_e32 v18, 0
	v_cvt_pk_fp8_f32 v19, v20, v21
	v_mov_b32_e32 v20, 0
	v_mov_b32_e32 v21, 0
	v_cvt_pk_fp8_f32 v18, v14, v15
	v_cvt_pk_fp8_f32 v20, v26, v27
	v_cvt_pk_fp8_f32 v21, v30, v31
	v_pk_mul_f32 v[10:11], v[126:127], s[26:27] op_sel_hi:[1,0]
	v_pk_mul_f32 v[22:23], v[122:123], s[26:27] op_sel_hi:[1,0]
	v_pk_mul_f32 v[24:25], v[118:119], s[26:27] op_sel_hi:[1,0]
	v_pk_mul_f32 v[28:29], v[114:115], s[26:27] op_sel_hi:[1,0]
	v_ashrrev_i32_e32 v13, 31, v12
	v_cvt_pk_fp8_f32 v18, v10, v11 op_sel:[0,0,1]
	v_cvt_pk_fp8_f32 v19, v22, v23 op_sel:[0,0,1]
	v_cvt_pk_fp8_f32 v20, v24, v25 op_sel:[0,0,1]
	v_cvt_pk_fp8_f32 v21, v28, v29 op_sel:[0,0,1]
	v_lshlrev_b64 v[10:11], 11, v[12:13]
	v_lshl_add_u64 v[10:11], s[18:19], 0, v[10:11]
	v_lshl_add_u64 v[10:11], v[10:11], 0, v[16:17]
	global_store_dwordx4 v[10:11], v[18:21], off
	v_pk_mul_f32 v[12:13], v[108:109], s[26:27] op_sel_hi:[1,0]
	v_mov_b32_e32 v10, 0
; #define PG8_BAR __builtin_amdgcn_s_barrier()
; __device__ __forceinline__ unsigned pk4_fp8(float a, float b, float c, float d) { int r = __builtin_amdgcn_cvt_pk_fp8_f32(a, b, 0, false); r = __builtin_amdgcn_cvt_pk_fp8_f32(c, d, r, true); return (unsigned)r; }
; template <class Epi, class Sched, bool ALIGN_EPI, bool FP8 = false>
; __device__ __forceinline__ void gemm_phase(PG8_LAS unsigned char* lds, const Gemm g, const Sched& S, const Epi& E, const int wid, const int lane) {
;     ...
;         if (!has_next) break;
; #pragma unroll
;         for (int a = 0; a < 2; ++a)
; #pragma unroll
;             for (int b = 0; b < 2; ++b)
; #pragma unroll
;                 for (int m = 0; m < 4; ++m)
; #pragma unroll
;                     for (int n = 0; n < 2; ++n) acc[a][b][m][n] = (f32x4){0.f, 0.f, 0.f, 0.f};
;         cur = nxt; cA = nA; cB = nB; ++ui;
;         if constexpr (ALIGN_EPI) { if (wr == 1) PG8_BAR; }
;     __device__ __forceinline__ void operator()(const f32x4 (&acc)[2][2][4][2], const Unit& u, int wr, int wc, int fr, int fq) const {
;     ...
; #pragma unroll
;         for (int ai = 0; ai < 2; ++ai)
; #pragma unroll
;             for (int m = 0; m < 4; ++m) { unsigned char* rowp = O + (size_t)drow[ai][m] * D + col0;
;                 const f32x4 a0 = acc[ai][0][m][0] * ysc, a1 = acc[ai][0][m][1] * ysc, b0 = acc[ai][1][m][0] * ysc, b1 = acc[ai][1][m][1] * ysc;
;                 v4u w; w.x = pk4_fp8(a0[0], a0[1], a0[2], a0[3]); w.y = pk4_fp8(a1[0], a1[1], a1[2], a1[3]); w.z = pk4_fp8(b0[0], b0[1], b0[2], b0[3]); w.w = pk4_fp8(b1[0], b1[1], b1[2], b1[3]);
;                 *(v4u*)rowp = w; }
	v_pk_mul_f32 v[20:21], v[104:105], s[26:27] op_sel_hi:[1,0]
	v_pk_mul_f32 v[24:25], v[100:101], s[26:27] op_sel_hi:[1,0]
	v_pk_mul_f32 v[28:29], v[96:97], s[26:27] op_sel_hi:[1,0]
	v_cvt_pk_fp8_f32 v10, v12, v13
	v_mov_b32_e32 v11, 0
	v_mov_b32_e32 v12, 0
	v_mov_b32_e32 v13, 0
	v_cvt_pk_fp8_f32 v11, v20, v21
	v_cvt_pk_fp8_f32 v12, v24, v25
	v_cvt_pk_fp8_f32 v13, v28, v29
	v_pk_mul_f32 v[14:15], v[110:111], s[26:27] op_sel_hi:[1,0]
	v_pk_mul_f32 v[18:19], v[106:107], s[26:27] op_sel_hi:[1,0]
	v_pk_mul_f32 v[22:23], v[102:103], s[26:27] op_sel_hi:[1,0]
	v_pk_mul_f32 v[26:27], v[98:99], s[26:27] op_sel_hi:[1,0]
	v_ashrrev_i32_e32 v9, 31, v8
	v_cvt_pk_fp8_f32 v10, v14, v15 op_sel:[0,0,1]
	v_cvt_pk_fp8_f32 v11, v18, v19 op_sel:[0,0,1]
	v_cvt_pk_fp8_f32 v12, v22, v23 op_sel:[0,0,1]
	v_cvt_pk_fp8_f32 v13, v26, v27 op_sel:[0,0,1]
	v_lshlrev_b64 v[8:9], 11, v[8:9]
	v_lshl_add_u64 v[8:9], s[18:19], 0, v[8:9]
	v_lshl_add_u64 v[8:9], v[8:9], 0, v[16:17]
	global_store_dwordx4 v[8:9], v[10:13], off
	v_mov_b32_e32 v8, 0
	v_pk_mul_f32 v[18:19], v[88:89], s[26:27] op_sel_hi:[1,0]
	v_pk_mul_f32 v[10:11], v[92:93], s[26:27] op_sel_hi:[1,0]
	v_pk_mul_f32 v[22:23], v[84:85], s[26:27] op_sel_hi:[1,0]
	v_pk_mul_f32 v[26:27], v[80:81], s[26:27] op_sel_hi:[1,0]
	v_cvt_pk_fp8_f32 v8, v10, v11
	v_mov_b32_e32 v9, 0
	v_mov_b32_e32 v10, 0
	v_mov_b32_e32 v11, 0
	v_cvt_pk_fp8_f32 v9, v18, v19
	v_cvt_pk_fp8_f32 v10, v22, v23
	v_cvt_pk_fp8_f32 v11, v26, v27
	v_pk_mul_f32 v[12:13], v[94:95], s[26:27] op_sel_hi:[1,0]
	v_pk_mul_f32 v[14:15], v[90:91], s[26:27] op_sel_hi:[1,0]
	v_pk_mul_f32 v[20:21], v[86:87], s[26:27] op_sel_hi:[1,0]
	v_pk_mul_f32 v[24:25], v[82:83], s[26:27] op_sel_hi:[1,0]
	v_ashrrev_i32_e32 v7, 31, v6
	v_cvt_pk_fp8_f32 v8, v12, v13 op_sel:[0,0,1]
	v_cvt_pk_fp8_f32 v9, v14, v15 op_sel:[0,0,1]
	v_cvt_pk_fp8_f32 v10, v20, v21 op_sel:[0,0,1]
	v_cvt_pk_fp8_f32 v11, v24, v25 op_sel:[0,0,1]
	v_lshlrev_b64 v[6:7], 11, v[6:7]
	v_lshl_add_u64 v[6:7], s[18:19], 0, v[6:7]
	v_lshl_add_u64 v[6:7], v[6:7], 0, v[16:17]
	global_store_dwordx4 v[6:7], v[8:11], off
	v_mov_b32_e32 v6, 0
	v_pk_mul_f32 v[14:15], v[72:73], s[26:27] op_sel_hi:[1,0]
	v_pk_mul_f32 v[8:9], v[76:77], s[26:27] op_sel_hi:[1,0]
	v_pk_mul_f32 v[20:21], v[68:69], s[26:27] op_sel_hi:[1,0]
	v_pk_mul_f32 v[24:25], v[64:65], s[26:27] op_sel_hi:[1,0]
	v_cvt_pk_fp8_f32 v6, v8, v9
	v_mov_b32_e32 v7, 0
	v_mov_b32_e32 v8, 0
	v_mov_b32_e32 v9, 0
	v_cvt_pk_fp8_f32 v7, v14, v15
	v_cvt_pk_fp8_f32 v8, v20, v21
	v_cvt_pk_fp8_f32 v9, v24, v25
	v_pk_mul_f32 v[10:11], v[78:79], s[26:27] op_sel_hi:[1,0]
	v_pk_mul_f32 v[12:13], v[74:75], s[26:27] op_sel_hi:[1,0]
	v_pk_mul_f32 v[18:19], v[70:71], s[26:27] op_sel_hi:[1,0]
	v_pk_mul_f32 v[22:23], v[66:67], s[26:27] op_sel_hi:[1,0]
	v_ashrrev_i32_e32 v5, 31, v4
	v_cvt_pk_fp8_f32 v6, v10, v11 op_sel:[0,0,1]
	v_cvt_pk_fp8_f32 v7, v12, v13 op_sel:[0,0,1]
	v_cvt_pk_fp8_f32 v8, v18, v19 op_sel:[0,0,1]
	v_cvt_pk_fp8_f32 v9, v22, v23 op_sel:[0,0,1]
	v_lshlrev_b64 v[4:5], 11, v[4:5]
	v_lshl_add_u64 v[4:5], s[18:19], 0, v[4:5]
	v_lshl_add_u64 v[4:5], v[4:5], 0, v[16:17]
	global_store_dwordx4 v[4:5], v[6:9], off
	v_mov_b32_e32 v4, 0
	v_pk_mul_f32 v[12:13], v[56:57], s[26:27] op_sel_hi:[1,0]
	v_pk_mul_f32 v[6:7], v[60:61], s[26:27] op_sel_hi:[1,0]
	v_pk_mul_f32 v[18:19], v[52:53], s[26:27] op_sel_hi:[1,0]
	v_pk_mul_f32 v[22:23], v[48:49], s[26:27] op_sel_hi:[1,0]
	v_cvt_pk_fp8_f32 v4, v6, v7
	v_mov_b32_e32 v5, 0
	v_mov_b32_e32 v6, 0
	v_mov_b32_e32 v7, 0
	v_cvt_pk_fp8_f32 v5, v12, v13
	v_cvt_pk_fp8_f32 v6, v18, v19
	v_cvt_pk_fp8_f32 v7, v22, v23
	v_pk_mul_f32 v[8:9], v[62:63], s[26:27] op_sel_hi:[1,0]
	v_pk_mul_f32 v[10:11], v[58:59], s[26:27] op_sel_hi:[1,0]
	v_pk_mul_f32 v[14:15], v[54:55], s[26:27] op_sel_hi:[1,0]
	v_pk_mul_f32 v[20:21], v[50:51], s[26:27] op_sel_hi:[1,0]
	v_ashrrev_i32_e32 v3, 31, v2
	v_cvt_pk_fp8_f32 v4, v8, v9 op_sel:[0,0,1]
	v_cvt_pk_fp8_f32 v5, v10, v11 op_sel:[0,0,1]
	v_cvt_pk_fp8_f32 v6, v14, v15 op_sel:[0,0,1]
	v_cvt_pk_fp8_f32 v7, v20, v21 op_sel:[0,0,1]
	v_lshlrev_b64 v[2:3], 11, v[2:3]
	v_lshl_add_u64 v[2:3], s[18:19], 0, v[2:3]
	v_lshl_add_u64 v[2:3], v[2:3], 0, v[16:17]
	global_store_dwordx4 v[2:3], v[4:7], off
	v_mov_b32_e32 v2, 0
	v_pk_mul_f32 v[10:11], v[40:41], s[26:27] op_sel_hi:[1,0]
	v_pk_mul_f32 v[4:5], v[44:45], s[26:27] op_sel_hi:[1,0]
	v_pk_mul_f32 v[14:15], v[36:37], s[26:27] op_sel_hi:[1,0]
	v_pk_mul_f32 v[20:21], v[32:33], s[26:27] op_sel_hi:[1,0]
	v_cvt_pk_fp8_f32 v2, v4, v5
	v_mov_b32_e32 v3, 0
	v_mov_b32_e32 v4, 0
	v_mov_b32_e32 v5, 0
	v_cvt_pk_fp8_f32 v3, v10, v11
	v_cvt_pk_fp8_f32 v4, v14, v15
	v_cvt_pk_fp8_f32 v5, v20, v21
	v_pk_mul_f32 v[6:7], v[46:47], s[26:27] op_sel_hi:[1,0]
	v_pk_mul_f32 v[8:9], v[42:43], s[26:27] op_sel_hi:[1,0]
	v_pk_mul_f32 v[12:13], v[38:39], s[26:27] op_sel_hi:[1,0]
	v_pk_mul_f32 v[18:19], v[34:35], s[26:27] op_sel_hi:[1,0]
	s_waitcnt lgkmcnt(0)
	v_ashrrev_i32_e32 v1, 31, v0
	v_cvt_pk_fp8_f32 v2, v6, v7 op_sel:[0,0,1]
	v_cvt_pk_fp8_f32 v3, v8, v9 op_sel:[0,0,1]
	v_cvt_pk_fp8_f32 v4, v12, v13 op_sel:[0,0,1]
	v_cvt_pk_fp8_f32 v5, v18, v19 op_sel:[0,0,1]
	v_lshlrev_b64 v[0:1], 11, v[0:1]
	v_lshl_add_u64 v[0:1], s[18:19], 0, v[0:1]
	v_lshl_add_u64 v[0:1], v[0:1], 0, v[16:17]
	s_and_b64 vcc, exec, s[4:5]
	s_mov_b64 s[4:5], -1
	global_store_dwordx4 v[0:1], v[2:5], off
	s_cbranch_vccnz .LBB0_838
	s_andn2_b64 vcc, exec, s[16:17]
	s_cbranch_vccnz .LBB0_837
	s_barrier
	s_branch .LBB0_837

; #define PG8_WAIT_V(n) asm volatile("s_waitcnt vmcnt(" #n ")" ::: "memory")
; #define PG8_WAIT_L(n) asm volatile("s_waitcnt lgkmcnt(" #n ")" ::: "memory")
; #define PG8_BAR __builtin_amdgcn_s_barrier()
; #define PG8_SCHED __builtin_amdgcn_sched_barrier(0)
; template <class Epi, class Sched, bool ALIGN_EPI, bool FP8 = false>
; __device__ __forceinline__ void gemm_phase(PG8_LAS unsigned char* lds, const Gemm g, const Sched& S, const Epi& E, const int wid, const int lane) {
;     ...
;             PG8_WAIT_V(8); PG8_WAIT_L(0); PG8_BAR; PG8_MMA(1, 0, At, B0); PG8_MMA(1, 1, At, B1); PG8_BAR; PG8_SCHED;
;         }
.Lp7b_w4j:
	s_waitcnt lgkmcnt(0)
	s_barrier
	s_setprio 1
	s_waitcnt lgkmcnt(6)
	v_mfma_scale_f32_16x16x128_f8f6f4 v[92:95], v[0:7], v[174:181], v[92:95], v170, v171 op_sel_hi:[0,0,0]
	v_mfma_scale_f32_16x16x128_f8f6f4 v[88:91], v[8:15], v[174:181], v[88:91], v170, v171 op_sel_hi:[0,0,0]
	s_waitcnt lgkmcnt(4)
	v_mfma_scale_f32_16x16x128_f8f6f4 v[76:79], v[0:7], v[182:189], v[76:79], v170, v171 op_sel_hi:[0,0,0]
	v_mfma_scale_f32_16x16x128_f8f6f4 v[72:75], v[8:15], v[182:189], v[72:75], v170, v171 op_sel_hi:[0,0,0]
	s_waitcnt lgkmcnt(2)
	v_mfma_scale_f32_16x16x128_f8f6f4 v[60:63], v[0:7], v[190:197], v[60:63], v170, v171 op_sel_hi:[0,0,0]
	v_mfma_scale_f32_16x16x128_f8f6f4 v[56:59], v[8:15], v[190:197], v[56:59], v170, v171 op_sel_hi:[0,0,0]
	s_waitcnt lgkmcnt(0)
	v_mfma_scale_f32_16x16x128_f8f6f4 v[44:47], v[0:7], v[198:205], v[44:47], v170, v171 op_sel_hi:[0,0,0]
	v_mfma_scale_f32_16x16x128_f8f6f4 v[40:43], v[8:15], v[198:205], v[40:43], v170, v171 op_sel_hi:[0,0,0]
	s_setprio 0
	s_setprio 1
	v_mfma_scale_f32_16x16x128_f8f6f4 v[84:87], v[16:23], v[174:181], v[84:87], v170, v171 op_sel_hi:[0,0,0]
	v_mfma_scale_f32_16x16x128_f8f6f4 v[80:83], v[24:31], v[174:181], v[80:83], v170, v171 op_sel_hi:[0,0,0]
	v_mfma_scale_f32_16x16x128_f8f6f4 v[68:71], v[16:23], v[182:189], v[68:71], v170, v171 op_sel_hi:[0,0,0]
	v_mfma_scale_f32_16x16x128_f8f6f4 v[64:67], v[24:31], v[182:189], v[64:67], v170, v171 op_sel_hi:[0,0,0]
	v_mfma_scale_f32_16x16x128_f8f6f4 v[52:55], v[16:23], v[190:197], v[52:55], v170, v171 op_sel_hi:[0,0,0]
	v_mfma_scale_f32_16x16x128_f8f6f4 v[48:51], v[24:31], v[190:197], v[48:51], v170, v171 op_sel_hi:[0,0,0]
	v_mfma_scale_f32_16x16x128_f8f6f4 v[36:39], v[16:23], v[198:205], v[36:39], v170, v171 op_sel_hi:[0,0,0]
	v_mfma_scale_f32_16x16x128_f8f6f4 v[32:35], v[24:31], v[198:205], v[32:35], v170, v171 op_sel_hi:[0,0,0]
	s_setprio 0
	s_barrier
	s_add_u32 s75, s75, 0x100
	s_addc_u32 s80, s80, 0
	s_add_u32 s81, s81, 0x100
	s_addc_u32 s82, s82, 0
	s_add_u32 s6, s6, 0x100
	s_addc_u32 s7, s7, 0
	s_cmp_ge_i32 s33, s52
	s_mov_b32 s8, s33
	s_cbranch_scc0 .LBB0_1762
